# HGRN chunk loop: the four loop-invariant rec_g loads hoisted out of the chunk loop (were an exposed round trip per chunk); on top of P5/P4a epilogue hoists + vm_wait direct branches + no-copy
# speedup vs baseline: 1.0070x; 1.0032x over previous
.LBB0_648:
	s_or_b64 exec, exec, s[26:27]
	v_mov_b32_e32 v2, s3
	s_waitcnt lgkmcnt(0)
	s_barrier
	ds_read_b32 v2, v2
	s_mov_b64 s[26:27], -1
	s_waitcnt lgkmcnt(0)
	v_cmp_gt_i32_e32 vcc, s2, v2
	v_readfirstlane_b32 s40, v2
	s_cbranch_vccz .LBB0_643
	global_load_dwordx4 v[194:197], v[110:111], off offset:48 nt
	global_load_dwordx4 v[198:201], v[110:111], off offset:32 nt
	global_load_dwordx4 v[202:205], v[110:111], off offset:16 nt
	global_load_dwordx4 v[206:209], v[110:111], off nt
	s_ashr_i32 s26, s40, 4
	s_lshl_b32 s27, s40, 7
	s_and_b32 s30, s27, 0x780
	s_ashr_i32 s27, s26, 31
	s_lshl_b64 s[38:39], s[26:27], 11
	s_mul_i32 s50, s26, 0x4800000
	v_readlane_b32 s28, v255, 4
	s_mul_hi_i32 s41, s26, 0x4800000
	v_readlane_b32 s29, v255, 5
	s_add_u32 s28, s28, s50
	v_or_b32_e32 v2, s30, v124
	s_addc_u32 s29, s29, s41
	s_lshl_b32 s49, s30, 1
	v_lshlrev_b32_e32 v2, 2, v2
	s_add_u32 s28, s28, s49
	global_load_dword v169, v2, s[84:85]
	s_addc_u32 s29, s29, 0
	v_mov_b32_e32 v2, v126
	v_mov_b32_e32 v108, v125
	v_mov_b32_e32 v3, v127
	v_mov_b32_e32 v10, v126
	v_lshl_add_u64 v[4:5], s[28:29], 0, v[108:109]
	v_add_co_u32_e32 v4, vcc, s42, v4
	v_mov_b32_e32 v3, v109
	s_nop 0
	v_addc_co_u32_e32 v5, vcc, 0, v5, vcc
	v_lshl_add_u64 v[2:3], s[28:29], 0, v[2:3]
	v_add_co_u32_e32 v6, vcc, s42, v2
	v_mov_b32_e32 v108, v125
	s_nop 0
	v_addc_co_u32_e32 v7, vcc, 0, v3, vcc
	v_mov_b32_e32 v11, v127
	global_load_dwordx4 v[2:5], v[4:5], off nt
	s_nop 0
	global_load_dwordx4 v[6:9], v[6:7], off nt
	v_mov_b32_e32 v18, v126
	v_lshl_add_u64 v[12:13], s[28:29], 0, v[108:109]
	v_add_co_u32_e32 v12, vcc, s43, v12
	v_mov_b32_e32 v11, v109
	s_nop 0
	v_addc_co_u32_e32 v13, vcc, 0, v13, vcc
	v_lshl_add_u64 v[10:11], s[28:29], 0, v[10:11]
	v_add_co_u32_e32 v14, vcc, s43, v10
	v_mov_b32_e32 v108, v125
	s_nop 0
	v_addc_co_u32_e32 v15, vcc, 0, v11, vcc
	v_mov_b32_e32 v19, v127
	global_load_dwordx4 v[10:13], v[12:13], off nt
	s_nop 0
	global_load_dwordx4 v[14:17], v[14:15], off nt
	v_mov_b32_e32 v26, v126
	v_lshl_add_u64 v[20:21], s[28:29], 0, v[108:109]
	v_add_co_u32_e32 v20, vcc, s44, v20
	v_mov_b32_e32 v19, v109
	s_nop 0
	v_addc_co_u32_e32 v21, vcc, 0, v21, vcc
	v_lshl_add_u64 v[18:19], s[28:29], 0, v[18:19]
	v_add_co_u32_e32 v22, vcc, s44, v18
	v_mov_b32_e32 v27, v125
	s_nop 0
	v_addc_co_u32_e32 v23, vcc, 0, v19, vcc
	v_mov_b32_e32 v28, v127
	global_load_dwordx4 v[18:21], v[20:21], off nt
	s_nop 0
	global_load_dwordx4 v[22:25], v[22:23], off nt
	global_load_dwordx4 v[38:41], v28, s[28:29] offset:16 nt
	global_load_dwordx4 v[46:49], v28, s[28:29] nt
	s_and_b32 s28, s40, 15
	s_lshl_b32 s28, s28, 8
	s_or_b32 s28, s50, s28
	s_add_u32 s50, s96, s28
	s_addc_u32 s51, s97, s41
	s_lshl_b64 s[26:27], s[26:27], 22
	s_or_b32 s26, s26, s30
	v_mov_b32_e32 v26, 0
	s_mov_b32 s49, 0
	v_lshl_add_u64 v[116:117], v[112:113], 0, s[30:31]
	v_mov_b32_e32 v119, s39
	v_or_b32_e32 v118, s38, v106
	v_lshl_add_u64 v[120:121], v[114:115], 0, s[26:27]
	v_mov_b64_e32 v[78:79], 0
	s_mov_b64 s[38:39], 0
	v_mov_b32_e32 v74, 0
	v_mov_b32_e32 v75, 0
	v_mov_b32_e32 v76, 0
	v_mov_b32_e32 v77, 0
	v_mov_b32_e32 v27, v26
	v_mov_b32_e32 v28, v26
	v_mov_b32_e32 v29, v26
	v_mov_b32_e32 v30, v26
	v_mov_b32_e32 v31, v26
	v_mov_b32_e32 v32, v26
	s_waitcnt vmcnt(8)
	v_sub_f32_e32 v170, 1.0, v169
	v_mov_b32_e32 v33, v26
	v_mov_b32_e32 v62, v26
	v_mov_b32_e32 v63, v26
	v_mov_b32_e32 v64, v26
	v_mov_b32_e32 v65, v26
	v_mov_b32_e32 v54, v26
	v_mov_b32_e32 v55, v26
	v_mov_b32_e32 v56, v26
	v_mov_b32_e32 v57, v26
	v_mov_b32_e32 v34, v26
	v_mov_b32_e32 v35, v26
	v_mov_b32_e32 v36, v26
	v_mov_b32_e32 v37, v26
	v_mov_b32_e32 v50, v26
	v_mov_b32_e32 v51, v26
	v_mov_b32_e32 v52, v26
	v_mov_b32_e32 v53, v26
	v_mov_b32_e32 v42, v26
	v_mov_b32_e32 v43, v26
	v_mov_b32_e32 v44, v26
	v_mov_b32_e32 v45, v26
	v_mov_b32_e32 v58, v26
	v_mov_b32_e32 v59, v26
	v_mov_b32_e32 v60, v26
	v_mov_b32_e32 v61, v26

.LBB0_666:
	ds_read_b64_tr_b16 v[78:79], v157 offset:53248
	ds_read_b64_tr_b16 v[80:81], v157 offset:54400
	ds_read_b64_tr_b16 v[74:75], v157 offset:62464
	ds_read_b64_tr_b16 v[76:77], v157 offset:63616
	ds_read_b128 v[82:85], v158
	ds_read_b128 v[86:89], v158 offset:2304
	ds_read_b128 v[90:93], v158 offset:4608
	ds_read_b128 v[94:97], v158 offset:4672
	ds_read_b128 v[98:101], v158 offset:6976
	v_add_u32_e32 v108, v137, v135
	v_add_u32_e32 v104, v137, v141
	s_waitcnt lgkmcnt(4)
	v_mfma_f32_16x16x32_bf16 v[82:85], v[82:85], v[78:81], 0
	v_add_u32_e32 v122, v142, v135
	v_add_u32_e32 v123, v143, v135
	v_add_u32_e32 v171, v144, v135
	s_waitcnt lgkmcnt(2)
	v_mfma_f32_16x16x32_bf16 v[90:93], v[90:93], v[78:81], 0
	s_lshl_b32 s30, s49, 6
	s_add_i32 s49, s49, 1
	s_add_u32 s38, s38, 0x240000
	s_waitcnt lgkmcnt(1)
	v_mfma_f32_16x16x32_bf16 v[90:93], v[94:97], v[74:77], v[90:93]
	ds_read_b128 v[94:97], v158 offset:6912
	s_addc_u32 s39, s39, 0
	s_mov_b64 s[26:27], 0x20000
	v_mfma_f32_16x16x32_bf16 v[86:89], v[86:89], v[78:81], 0
	v_lshl_add_u64 v[120:121], v[120:121], 0, s[26:27]
	s_cmp_lg_u32 s38, 0x4800000
	s_waitcnt lgkmcnt(0)
	v_mfma_f32_16x16x32_bf16 v[94:97], v[94:97], v[78:81], 0
	v_mfma_f32_16x16x32_bf16 v[94:97], v[98:101], v[74:77], v[94:97]
	v_cvt_pk_bf16_f32 v98, v26, v27
	v_cvt_pk_bf16_f32 v99, v28, v29
	v_cvt_pk_bf16_f32 v100, v30, v31
	v_cvt_pk_bf16_f32 v101, v32, v33
	ds_read_b64 v[102:103], v108
	ds_read_b64 v[104:105], v104
	s_waitcnt lgkmcnt(0)
	v_mfma_f32_16x16x32_bf16 v[82:85], v[102:105], v[98:101], v[82:85]
	v_add_u32_e32 v104, v142, v141
	ds_read_b64 v[102:103], v122
	ds_read_b64 v[104:105], v104
	s_waitcnt lgkmcnt(0)
	v_mfma_f32_16x16x32_bf16 v[86:89], v[102:105], v[98:101], v[86:89]
	v_add_u32_e32 v104, v143, v141
	ds_read_b64 v[102:103], v123
	ds_read_b64 v[104:105], v104
	s_waitcnt lgkmcnt(0)
	v_mfma_f32_16x16x32_bf16 v[90:93], v[102:105], v[98:101], v[90:93]
	v_add_u32_e32 v104, v144, v141
	ds_read_b64 v[102:103], v171
	ds_read_b64 v[104:105], v104
	s_waitcnt lgkmcnt(0)
	v_mfma_f32_16x16x32_bf16 v[94:97], v[102:105], v[98:101], v[94:97]
	v_add_u32_e32 v102, v137, v145
	v_add_u32_e32 v104, v137, v146
	v_cvt_pk_bf16_f32 v98, v62, v63
	v_cvt_pk_bf16_f32 v99, v64, v65
	v_cvt_pk_bf16_f32 v100, v54, v55
	v_cvt_pk_bf16_f32 v101, v56, v57
	ds_read_b64 v[102:103], v102
	ds_read_b64 v[104:105], v104
	s_waitcnt lgkmcnt(0)
	v_mfma_f32_16x16x32_bf16 v[82:85], v[102:105], v[98:101], v[82:85]
	v_add_u32_e32 v102, v142, v145
	v_add_u32_e32 v104, v142, v146
	ds_read_b64 v[102:103], v102
	ds_read_b64 v[104:105], v104
	s_waitcnt lgkmcnt(0)
	v_mfma_f32_16x16x32_bf16 v[86:89], v[102:105], v[98:101], v[86:89]
	v_add_u32_e32 v102, v143, v145
	v_add_u32_e32 v104, v143, v146
	ds_read_b64 v[102:103], v102
	ds_read_b64 v[104:105], v104
	s_waitcnt lgkmcnt(0)
	v_mfma_f32_16x16x32_bf16 v[90:93], v[102:105], v[98:101], v[90:93]
	v_add_u32_e32 v102, v144, v145
	v_add_u32_e32 v104, v144, v146
	ds_read_b64 v[102:103], v102
	ds_read_b64 v[104:105], v104
	s_waitcnt lgkmcnt(0)
	v_mfma_f32_16x16x32_bf16 v[94:97], v[102:105], v[98:101], v[94:97]
	v_cvt_pk_bf16_f32 v98, v34, v35
	v_cvt_pk_bf16_f32 v99, v36, v37
	v_cvt_pk_bf16_f32 v100, v50, v51
	v_cvt_pk_bf16_f32 v101, v52, v53
	ds_read2_b64 v[102:105], v108 offset0:16 offset1:20
	s_waitcnt lgkmcnt(0)
	v_mfma_f32_16x16x32_bf16 v[82:85], v[102:105], v[98:101], v[82:85]
	ds_read2_b64 v[102:105], v122 offset0:16 offset1:20
	s_waitcnt lgkmcnt(0)
	v_mfma_f32_16x16x32_bf16 v[86:89], v[102:105], v[98:101], v[86:89]
	ds_read2_b64 v[102:105], v123 offset0:16 offset1:20
	s_waitcnt lgkmcnt(0)
	v_mfma_f32_16x16x32_bf16 v[90:93], v[102:105], v[98:101], v[90:93]
	ds_read2_b64 v[102:105], v171 offset0:16 offset1:20
	s_waitcnt lgkmcnt(0)
	v_mfma_f32_16x16x32_bf16 v[94:97], v[102:105], v[98:101], v[94:97]
	v_cvt_pk_bf16_f32 v98, v42, v43
	v_cvt_pk_bf16_f32 v99, v44, v45
	v_cvt_pk_bf16_f32 v100, v58, v59
	v_cvt_pk_bf16_f32 v101, v60, v61
	ds_read2_b64 v[102:105], v108 offset0:24 offset1:28
	s_waitcnt lgkmcnt(0)
	v_mfma_f32_16x16x32_bf16 v[82:85], v[102:105], v[98:101], v[82:85]
	ds_read2_b64 v[102:105], v122 offset0:24 offset1:28
	s_waitcnt lgkmcnt(0)
	v_mfma_f32_16x16x32_bf16 v[86:89], v[102:105], v[98:101], v[86:89]
	ds_read2_b64 v[102:105], v123 offset0:24 offset1:28
	v_lshl_add_u64 v[122:123], v[118:119], 0, s[30:31]
	s_waitcnt lgkmcnt(0)
	v_mfma_f32_16x16x32_bf16 v[90:93], v[102:105], v[98:101], v[90:93]
	ds_read2_b64 v[102:105], v171 offset0:24 offset1:28
	ds_write2_b32 v159, v82, v83 offset1:132
	v_add_u32_e32 v82, 0x400, v159
	s_waitcnt lgkmcnt(1)
	v_mfma_f32_16x16x32_bf16 v[94:97], v[102:105], v[98:101], v[94:97]
	ds_write2_b32 v82, v84, v85 offset0:8 offset1:140
	ds_write_b32 v160, v86
	v_add_u32_e32 v82, 0x2200, v159
	ds_write2_b32 v82, v87, v88 offset0:68 offset1:200
	ds_write_b32 v159, v89 offset:10032
	ds_write_b32 v160, v90 offset:8448
	v_add_u32_e32 v82, 0x4400, v159
	ds_write2_b32 v82, v91, v92 offset0:4 offset1:136
	ds_write_b32 v159, v93 offset:18480
	ds_write_b32 v160, v94 offset:16896
	v_add_u32_e32 v82, 0x6400, v159
	ds_write2_b32 v82, v95, v96 offset0:68 offset1:200
	ds_write_b32 v159, v97 offset:26928
	v_add_u32_e32 v92, 0x1c000, v134
	ds_read_b128 v[82:85], v92
	s_waitcnt lgkmcnt(0)
	v_pk_mul_f32 v[26:27], v[26:27], v[82:83]
	v_add_u32_e32 v82, v140, v136
	v_pk_mul_f32 v[28:29], v[28:29], v[84:85]
	ds_read_b64_tr_b16 v[86:87], v82 offset:35968
	ds_read_b64_tr_b16 v[84:85], v82 offset:34816
	ds_read_b64_tr_b16 v[88:89], v82 offset:34848
	s_waitcnt lgkmcnt(1)
	v_mfma_f32_16x16x32_bf16 v[26:29], v[84:87], v[78:81], v[26:29]
	ds_read_b64_tr_b16 v[84:85], v82 offset:44032
	ds_read_b64_tr_b16 v[86:87], v82 offset:45184
	ds_read_b64_tr_b16 v[90:91], v82 offset:36000
	s_waitcnt lgkmcnt(1)
	v_mfma_f32_16x16x32_bf16 v[26:29], v[84:87], v[74:77], v[26:29]
	ds_read_b128 v[84:87], v92 offset:64
	s_waitcnt lgkmcnt(0)
	v_pk_mul_f32 v[30:31], v[30:31], v[84:85]
	v_pk_mul_f32 v[32:33], v[32:33], v[86:87]
	ds_read_b64_tr_b16 v[84:85], v82 offset:44064
	ds_read_b64_tr_b16 v[86:87], v82 offset:45216
	v_mfma_f32_16x16x32_bf16 v[30:33], v[88:91], v[78:81], v[30:33]
	s_waitcnt lgkmcnt(0)
	v_mfma_f32_16x16x32_bf16 v[30:33], v[84:87], v[74:77], v[30:33]
	ds_read_b128 v[84:87], v92 offset:128
	s_waitcnt lgkmcnt(0)
	v_pk_mul_f32 v[62:63], v[62:63], v[84:85]
	v_pk_mul_f32 v[64:65], v[64:65], v[86:87]
	ds_read_b64_tr_b16 v[84:85], v82 offset:34880
	ds_read_b64_tr_b16 v[86:87], v82 offset:36032
	s_waitcnt lgkmcnt(0)
	v_mfma_f32_16x16x32_bf16 v[62:65], v[84:87], v[78:81], v[62:65]
	ds_read_b64_tr_b16 v[84:85], v82 offset:44096
	ds_read_b64_tr_b16 v[86:87], v82 offset:45248
	s_waitcnt lgkmcnt(0)
	v_mfma_f32_16x16x32_bf16 v[62:65], v[84:87], v[74:77], v[62:65]
	ds_read_b128 v[84:87], v92 offset:192
	s_waitcnt lgkmcnt(0)
	v_pk_mul_f32 v[54:55], v[54:55], v[84:85]
	v_pk_mul_f32 v[56:57], v[56:57], v[86:87]
	ds_read_b64_tr_b16 v[84:85], v82 offset:34912
	ds_read_b64_tr_b16 v[86:87], v82 offset:36064
	s_waitcnt lgkmcnt(0)
	v_mfma_f32_16x16x32_bf16 v[54:57], v[84:87], v[78:81], v[54:57]
	ds_read_b64_tr_b16 v[84:85], v82 offset:44128
	ds_read_b64_tr_b16 v[86:87], v82 offset:45280
	s_waitcnt lgkmcnt(0)
	v_mfma_f32_16x16x32_bf16 v[54:57], v[84:87], v[74:77], v[54:57]
	ds_read_b128 v[84:87], v92 offset:256
	s_waitcnt lgkmcnt(0)
	v_pk_mul_f32 v[34:35], v[34:35], v[84:85]
	v_pk_mul_f32 v[36:37], v[36:37], v[86:87]
	ds_read_b64_tr_b16 v[84:85], v82 offset:34944
	ds_read_b64_tr_b16 v[86:87], v82 offset:36096
	s_waitcnt lgkmcnt(0)
	v_mfma_f32_16x16x32_bf16 v[34:37], v[84:87], v[78:81], v[34:37]
	ds_read_b64_tr_b16 v[84:85], v82 offset:44160
	ds_read_b64_tr_b16 v[86:87], v82 offset:45312
	s_waitcnt lgkmcnt(0)
	v_mfma_f32_16x16x32_bf16 v[34:37], v[84:87], v[74:77], v[34:37]
	ds_read_b128 v[84:87], v92 offset:320
	s_waitcnt lgkmcnt(0)
	v_pk_mul_f32 v[50:51], v[50:51], v[84:85]
	v_pk_mul_f32 v[52:53], v[52:53], v[86:87]
	ds_read_b64_tr_b16 v[84:85], v82 offset:34976
	ds_read_b64_tr_b16 v[86:87], v82 offset:36128
	s_waitcnt lgkmcnt(0)
	v_mfma_f32_16x16x32_bf16 v[50:53], v[84:87], v[78:81], v[50:53]
	ds_read_b64_tr_b16 v[84:85], v82 offset:44192
	ds_read_b64_tr_b16 v[86:87], v82 offset:45344
	s_waitcnt lgkmcnt(0)
	v_mfma_f32_16x16x32_bf16 v[50:53], v[84:87], v[74:77], v[50:53]
	ds_read_b128 v[84:87], v92 offset:384
	s_waitcnt lgkmcnt(0)
	v_pk_mul_f32 v[42:43], v[42:43], v[84:85]
	v_pk_mul_f32 v[44:45], v[44:45], v[86:87]
	ds_read_b64_tr_b16 v[84:85], v82 offset:35008
	ds_read_b64_tr_b16 v[86:87], v82 offset:36160
	s_waitcnt lgkmcnt(0)
	v_mfma_f32_16x16x32_bf16 v[42:45], v[84:87], v[78:81], v[42:45]
	ds_read_b64_tr_b16 v[84:85], v82 offset:44224
	ds_read_b64_tr_b16 v[86:87], v82 offset:45376
	s_waitcnt lgkmcnt(0)
	v_mfma_f32_16x16x32_bf16 v[42:45], v[84:87], v[74:77], v[42:45]
	ds_read_b128 v[84:87], v92 offset:448
	s_waitcnt lgkmcnt(0)
	v_pk_mul_f32 v[58:59], v[58:59], v[84:85]
	v_pk_mul_f32 v[60:61], v[60:61], v[86:87]
	ds_read_b64_tr_b16 v[84:85], v82 offset:35040
	ds_read_b64_tr_b16 v[86:87], v82 offset:36192
	s_waitcnt lgkmcnt(0)
	v_mfma_f32_16x16x32_bf16 v[58:61], v[84:87], v[78:81], v[58:61]
	ds_read_b64_tr_b16 v[78:79], v82 offset:44256
	ds_read_b64_tr_b16 v[80:81], v82 offset:45408
	s_waitcnt lgkmcnt(0)
	s_barrier
	s_waitcnt lgkmcnt(0)
	v_mfma_f32_16x16x32_bf16 v[58:61], v[78:81], v[74:77], v[58:61]
	ds_read_b128 v[86:89], v161
	ds_read_b128 v[82:85], v161 offset:16
	ds_read_b128 v[78:81], v161 offset:32
	ds_read_b128 v[74:77], v161 offset:48
	s_waitcnt lgkmcnt(3)
	v_pk_mul_f32 v[90:91], v[88:89], v[88:89]
	v_pk_mul_f32 v[92:93], v[86:87], v[86:87]
	s_nop 0
	v_pk_mov_b32 v[94:95], v[92:93], v[90:91] op_sel:[1,0]
	v_mov_b32_e32 v93, v91
	v_pk_add_f32 v[90:91], v[94:95], v[92:93]
	s_waitcnt lgkmcnt(2)
	v_pk_mul_f32 v[92:93], v[84:85], v[84:85]
	v_pk_mul_f32 v[94:95], v[82:83], v[82:83]
	v_pk_add_f32 v[90:91], v[90:91], v[90:91] op_sel:[0,1] op_sel_hi:[1,0]
	v_pk_mov_b32 v[96:97], v[94:95], v[92:93] op_sel:[1,0]
	v_mov_b32_e32 v95, v93
	v_pk_add_f32 v[92:93], v[96:97], v[94:95]
	s_waitcnt lgkmcnt(0)
	v_mul_f32_e32 v94, v74, v74
	v_mul_f32_e32 v95, v75, v75
	v_pk_add_f32 v[92:93], v[92:93], v[92:93] op_sel:[0,1] op_sel_hi:[1,0]
	v_mov_b32_e32 v91, v94
	v_mov_b32_e32 v93, v95
	v_pk_add_f32 v[90:91], v[90:91], v[92:93]
	v_mul_f32_e32 v92, v79, v79
	v_mul_f32_e32 v94, v81, v81
	v_mul_f32_e32 v96, v76, v76
	v_mul_f32_e32 v97, v77, v77
	v_pk_fma_f32 v[92:93], v[78:79], v[78:79], v[92:93] op_sel_hi:[1,1,0]
	v_pk_fma_f32 v[94:95], v[80:81], v[80:81], v[94:95] op_sel_hi:[1,1,0]
	v_mov_b32_e32 v93, v96
	v_mov_b32_e32 v95, v97
	v_pk_add_f32 v[92:93], v[92:93], v[94:95]
	s_nop 0
	v_pk_add_f32 v[90:91], v[90:91], v[92:93]
	v_and_b32_e32 v92, 64, v166
	v_add_f32_e32 v90, v90, v91
	v_xor_b32_e32 v91, 1, v166
	v_add_u32_e32 v92, 64, v92
	v_cmp_lt_i32_e32 vcc, v91, v92
	s_nop 1
	v_cndmask_b32_e32 v91, v166, v91, vcc
	v_lshlrev_b32_e32 v91, 2, v91
	ds_bpermute_b32 v91, v91, v90
	s_waitcnt lgkmcnt(0)
	v_add_f32_e32 v90, v90, v91
	v_xor_b32_e32 v91, 2, v166
	v_cmp_lt_i32_e32 vcc, v91, v92
	s_nop 1
	v_cndmask_b32_e32 v91, v166, v91, vcc
	v_lshlrev_b32_e32 v91, 2, v91
	ds_bpermute_b32 v91, v91, v90
	s_waitcnt lgkmcnt(0)
	v_add_f32_e32 v90, v90, v91
	v_xor_b32_e32 v91, 4, v166
	v_cmp_lt_i32_e32 vcc, v91, v92
	s_nop 1
	v_cndmask_b32_e32 v91, v166, v91, vcc
	v_lshlrev_b32_e32 v91, 2, v91
	ds_bpermute_b32 v91, v91, v90
	s_waitcnt lgkmcnt(0)
	v_add_f32_e32 v90, v90, v91
	v_fmamk_f32 v90, v90, 0x3c000000, v162
	v_cmp_gt_f32_e32 vcc, s45, v90
	v_mul_f32_e32 v91, 0x4b800000, v90
	s_nop 0
	v_cndmask_b32_e32 v90, v90, v91, vcc
	v_rsq_f32_e32 v90, v90
	s_nop 0
	v_mul_f32_e32 v91, 0x45800000, v90
	v_cndmask_b32_e32 v108, v90, v91, vcc
	v_mov_b64_e32 v[90:91], v[194:195]
	v_mov_b64_e32 v[92:93], v[196:197]
	v_mov_b64_e32 v[94:95], v[198:199]
	v_mov_b64_e32 v[96:97], v[200:201]
	v_mov_b64_e32 v[98:99], v[202:203]
	v_mov_b64_e32 v[100:101], v[204:205]
	v_mov_b64_e32 v[102:103], v[206:207]
	v_mov_b64_e32 v[104:105], v[208:209]
	v_mul_f32_e32 v86, v86, v108
	v_mul_f32_e32 v87, v87, v108
	v_mul_f32_e32 v83, v83, v108
	v_mul_f32_e32 v79, v79, v108
	v_mul_f32_e32 v74, v74, v108
	v_mul_f32_e32 v82, v82, v108
	v_mul_f32_e32 v78, v78, v108
	s_waitcnt vmcnt(3)
	v_mul_f32_e32 v74, v90, v74
	s_waitcnt vmcnt(2)
	v_mul_f32_e32 v79, v95, v79
	s_waitcnt vmcnt(1)
	v_mul_f32_e32 v83, v99, v83
	s_waitcnt vmcnt(0)
	v_mul_f32_e32 v86, v102, v86
	v_lshlrev_b32_e32 v102, 16, v46
	v_mul_f32_e32 v87, v103, v87
	v_and_b32_e32 v46, 0xffff0000, v46
	v_mul_f32_e32 v46, v87, v46
	v_mul_f32_e32 v87, v88, v108
	v_mul_f32_e32 v87, v104, v87
	v_lshlrev_b32_e32 v88, 16, v47
	v_mul_f32_e32 v87, v87, v88
	v_mul_f32_e32 v88, v89, v108
	v_mul_f32_e32 v88, v105, v88
	v_and_b32_e32 v47, 0xffff0000, v47
	v_mul_f32_e32 v47, v88, v47
	v_lshlrev_b32_e32 v88, 16, v48
	v_and_b32_e32 v48, 0xffff0000, v48
	v_mul_f32_e32 v48, v83, v48
	v_mul_f32_e32 v83, v84, v108
	v_mul_f32_e32 v83, v100, v83
	v_lshlrev_b32_e32 v84, 16, v49
	v_mul_f32_e32 v83, v83, v84
	v_mul_f32_e32 v84, v85, v108
	v_mul_f32_e32 v84, v101, v84
	v_and_b32_e32 v49, 0xffff0000, v49
	v_mul_f32_e32 v49, v84, v49
	v_lshlrev_b32_e32 v84, 16, v38
	v_and_b32_e32 v38, 0xffff0000, v38
	v_mul_f32_e32 v38, v79, v38
	v_mul_f32_e32 v79, v80, v108
	v_mul_f32_e32 v79, v96, v79
	v_lshlrev_b32_e32 v80, 16, v39
	v_mul_f32_e32 v79, v79, v80
	v_mul_f32_e32 v80, v81, v108
	v_mul_f32_e32 v80, v97, v80
	v_and_b32_e32 v39, 0xffff0000, v39
	v_mul_f32_e32 v39, v80, v39
	v_lshlrev_b32_e32 v80, 16, v40
	v_mul_f32_e32 v80, v74, v80
	v_mul_f32_e32 v74, v75, v108
	v_mul_f32_e32 v74, v91, v74
	v_and_b32_e32 v40, 0xffff0000, v40
	v_mul_f32_e32 v40, v74, v40
	v_mul_f32_e32 v74, v76, v108
	v_mul_f32_e32 v74, v92, v74
	v_lshlrev_b32_e32 v75, 16, v41
	v_mul_f32_e32 v81, v74, v75
	v_mul_f32_e32 v74, v77, v108
	v_mul_f32_e32 v82, v98, v82
	v_mul_f32_e32 v78, v94, v78
	v_mul_f32_e32 v74, v93, v74
	v_and_b32_e32 v41, 0xffff0000, v41
	v_mul_f32_e32 v86, v86, v102
	v_mul_f32_e32 v82, v82, v88
	v_mul_f32_e32 v78, v78, v84
	v_mul_f32_e32 v41, v74, v41
	v_mov_b32_e32 v74, 0
	v_mov_b32_e32 v75, 0
	v_mov_b32_e32 v76, 0
	v_mov_b32_e32 v77, 0
	v_cvt_pk_fp8_f32 v74, v86, v46
	v_cvt_pk_fp8_f32 v75, v82, v48
	v_cvt_pk_fp8_f32 v76, v78, v38
	v_cvt_pk_fp8_f32 v77, v80, v40
	v_cvt_pk_fp8_f32 v74, v87, v47 op_sel:[0,0,1]
	v_cvt_pk_fp8_f32 v75, v83, v49 op_sel:[0,0,1]
	v_cvt_pk_fp8_f32 v76, v79, v39 op_sel:[0,0,1]
	v_cvt_pk_fp8_f32 v77, v81, v41 op_sel:[0,0,1]
	v_lshlrev_b64 v[38:39], 11, v[122:123]
	v_lshl_add_u64 v[78:79], v[116:117], 0, v[38:39]
	s_cbranch_scc0 .LBB0_642
	v_mov_b64_e32 v[38:39], v[70:71]
	v_mov_b64_e32 v[46:47], v[66:67]
	v_mov_b64_e32 v[40:41], v[72:73]
	v_mov_b64_e32 v[48:49], v[68:69]
	s_branch .LBB0_650
